# v57 + attention lazy-rescale test shortened: branch on the scalar all-lanes compare instead of a second vector compare (2 sites)
# speedup vs baseline: 1.0020x; 1.0020x over previous
; template <int OFF> __device__ __forceinline__ bf16x8 k_read(int kb) { bf16x8 r; asm volatile("ds_read_b128 %0, %1 offset:%2" : "=&v"(r) : "v"(kb), "i"(OFF) : "memory"); return r; }
; #define QK_STEP(D, X, Y, NEXT, N) do { K_WAIT(N, X, Y); \
;         p0 = __builtin_amdgcn_mfma_f32_32x32x16_bf16(X, qr[D], p0, 0, 0, 0); p1 = __builtin_amdgcn_mfma_f32_32x32x16_bf16(Y, qr[D], p1, 0, 0, 0); \
;         if constexpr ((NEXT) < 12) { X = k_read<(NEXT) * 32>(kb); Y = k_read<R1 + (NEXT) * 32>(kb); } } while (0)
; __device__ __forceinline__ void partialSM(f32x16& p0, f32x16& p1, float& m_reg, float& mn, float& alpha) {
;     constexpr float C = SCALE * 1.4426950408889634f;
;     float pmax = p0[0];
; #pragma unroll
;     for (int r = 1; r < 16; ++r) pmax = fmaxf(pmax, p0[r]);
; #pragma unroll
;     for (int r = 0; r < 16; ++r) pmax = fmaxf(pmax, p1[r]);
;     { auto rr = __builtin_amdgcn_permlane32_swap(__float_as_uint(pmax), __float_as_uint(pmax), false, false);
;       pmax = fmaxf(__uint_as_float(rr[0]), __uint_as_float(rr[1])); }
;     if (__builtin_expect(__all(pmax - m_reg <= THR / SCALE), 1)) { mn = m_reg; alpha = 1.f; }
;     else { mn = fmaxf(m_reg, pmax); alpha = __builtin_amdgcn_exp2f((m_reg - mn) * C); m_reg = mn; }
; __device__ __forceinline__ void qkt(f32x16& p0, f32x16& p1, const unsigned char* Ks, const bf16x8* qr, int r32, int hi) {
;     const int kb = (int)(uintptr_t)Ks + r32 * KPITCH + hi * 16;
;     constexpr int R1 = 32 * KPITCH;
;     p0 = f32x16{}; p1 = f32x16{};
;     bf16x8 a0 = k_read<0>(kb), a1 = k_read<R1>(kb), a2 = k_read<32>(kb), a3 = k_read<R1 + 32>(kb), a4 = k_read<64>(kb), a5 = k_read<R1 + 64>(kb);
;     ...
;     QK_STEP(0, a0, a1, 3, 4); QK_STEP(1, a2, a3, 4, 4); QK_STEP(2, a4, a5, 5, 4);
;     QK_STEP(3, a0, a1, 6, 4); QK_STEP(4, a2, a3, 7, 4); QK_STEP(5, a4, a5, 8, 4);
;     QK_STEP(6, a0, a1, 9, 4); QK_STEP(7, a2, a3, 10, 4); QK_STEP(8, a4, a5, 11, 4);
;     QK_STEP(9, a0, a1, 12, 4); QK_STEP(10, a2, a3, 12, 2); QK_STEP(11, a4, a5, 12, 0);
.LBB0_1001:
	s_bitcmp1_b32 s0, 0
	s_cselect_b32 s49, 0x6400, 0
	s_cmp_lg_u32 0, -1
	s_cselect_b32 s0, 0, 0
	s_add_i32 s0, s0, s49
	v_add_u32_e32 v174, s0, v178
	ds_read_b128 v[64:67], v174 offset:0
	ds_read_b128 v[68:71], v174 offset:0x3200
	ds_read_b128 v[180:183], v174 offset:32
	ds_read_b128 v[184:187], v174 offset:0x3220
	ds_read_b128 v[188:191], v174 offset:64
	ds_read_b128 v[192:195], v174 offset:0x3240
	s_nop 0
	s_waitcnt lgkmcnt(4)
	ds_read_b128 v[196:199], v174 offset:0x60
	ds_read_b128 v[200:203], v174 offset:0x3260
	s_waitcnt lgkmcnt(4)
	s_nop 0
	v_mfma_f32_32x32x16_bf16 v[80:95], v[64:67], v[142:145], 0
	v_mfma_f32_32x32x16_bf16 v[64:79], v[68:71], v[142:145], 0
	v_mfma_f32_32x32x16_bf16 v[80:95], v[180:183], v[138:141], v[80:95]
	ds_read_b128 v[180:183], v174 offset:0x80
	v_mfma_f32_32x32x16_bf16 v[64:79], v[184:187], v[138:141], v[64:79]
	ds_read_b128 v[184:187], v174 offset:0x3280
	s_waitcnt lgkmcnt(4)
	s_nop 0
	v_mfma_f32_32x32x16_bf16 v[80:95], v[188:191], v[134:137], v[80:95]
	ds_read_b128 v[188:191], v174 offset:0xa0
	v_mfma_f32_32x32x16_bf16 v[64:79], v[192:195], v[134:137], v[64:79]
	ds_read_b128 v[192:195], v174 offset:0x32a0
	s_waitcnt lgkmcnt(4)
	s_nop 0
	v_mfma_f32_32x32x16_bf16 v[80:95], v[196:199], v[130:133], v[80:95]
	ds_read_b128 v[196:199], v174 offset:0xc0
	v_mfma_f32_32x32x16_bf16 v[64:79], v[200:203], v[130:133], v[64:79]
	ds_read_b128 v[200:203], v174 offset:0x32c0
	s_waitcnt lgkmcnt(4)
	s_nop 0
	v_mfma_f32_32x32x16_bf16 v[80:95], v[180:183], v[126:129], v[80:95]
	ds_read_b128 v[180:183], v174 offset:0xe0
	v_mfma_f32_32x32x16_bf16 v[64:79], v[184:187], v[126:129], v[64:79]
	ds_read_b128 v[184:187], v174 offset:0x32e0
	s_waitcnt lgkmcnt(4)
	s_nop 0
	v_mfma_f32_32x32x16_bf16 v[80:95], v[188:191], v[122:125], v[80:95]
	ds_read_b128 v[188:191], v174 offset:0x100
	v_mfma_f32_32x32x16_bf16 v[64:79], v[192:195], v[122:125], v[64:79]
	ds_read_b128 v[192:195], v174 offset:0x3300
	s_waitcnt lgkmcnt(4)
	s_nop 0
	v_mfma_f32_32x32x16_bf16 v[80:95], v[196:199], v[118:121], v[80:95]
	ds_read_b128 v[196:199], v174 offset:0x120
	v_mfma_f32_32x32x16_bf16 v[64:79], v[200:203], v[118:121], v[64:79]
	ds_read_b128 v[200:203], v174 offset:0x3320
	s_waitcnt lgkmcnt(4)
	s_nop 0
	v_mfma_f32_32x32x16_bf16 v[80:95], v[180:183], v[114:117], v[80:95]
	ds_read_b128 v[180:183], v174 offset:0x140
	v_mfma_f32_32x32x16_bf16 v[64:79], v[184:187], v[114:117], v[64:79]
	ds_read_b128 v[184:187], v174 offset:0x3340
	s_waitcnt lgkmcnt(4)
	s_nop 0
	v_mfma_f32_32x32x16_bf16 v[80:95], v[188:191], v[110:113], v[80:95]
	ds_read_b128 v[188:191], v174 offset:0x160
	v_mfma_f32_32x32x16_bf16 v[64:79], v[192:195], v[110:113], v[64:79]
	ds_read_b128 v[192:195], v174 offset:0x3360
	s_waitcnt lgkmcnt(4)
	s_waitcnt lgkmcnt(2)
	s_nop 0
	s_waitcnt lgkmcnt(0)
	v_add_u32_e32 v207, s49, v172
	ds_read_b64_tr_b16 v[220:221], v207 offset:0
	ds_read_b64_tr_b16 v[222:223], v207 offset:1600
	ds_read_b64_tr_b16 v[224:225], v207 offset:64
	ds_read_b64_tr_b16 v[226:227], v207 offset:1664
	ds_read_b64_tr_b16 v[228:229], v207 offset:128
	ds_read_b64_tr_b16 v[230:231], v207 offset:1728
	ds_read_b64_tr_b16 v[232:233], v207 offset:192
	ds_read_b64_tr_b16 v[234:235], v207 offset:1792
	ds_read_b64_tr_b16 v[236:237], v207 offset:6400
	ds_read_b64_tr_b16 v[238:239], v207 offset:8000
	ds_read_b64_tr_b16 v[240:241], v207 offset:6464
	ds_read_b64_tr_b16 v[242:243], v207 offset:8064
	ds_read_b64_tr_b16 v[244:245], v207 offset:6528
	ds_read_b64_tr_b16 v[246:247], v207 offset:8128
	ds_read_b64_tr_b16 v[248:249], v207 offset:6592
	ds_read_b64_tr_b16 v[250:251], v207 offset:8192
	v_mfma_f32_32x32x16_bf16 v[80:95], v[196:199], v[106:109], v[80:95]
	v_mfma_f32_32x32x16_bf16 v[80:95], v[180:183], v[102:105], v[80:95]
	v_max_f32_e32 v181, v173, v173
	v_mfma_f32_32x32x16_bf16 v[64:79], v[200:203], v[106:109], v[64:79]
	v_mfma_f32_32x32x16_bf16 v[80:95], v[188:191], v[98:101], v[80:95]
	v_mfma_f32_32x32x16_bf16 v[64:79], v[184:187], v[102:105], v[64:79]
	s_nop 10
	v_max_f32_e32 v174, v81, v81
	v_max_f32_e32 v180, v80, v80
	v_max_f32_e32 v174, v180, v174
	v_max3_f32 v174, v174, v82, v83
	v_max3_f32 v174, v174, v84, v85
	v_max3_f32 v174, v174, v86, v87
	v_max3_f32 v174, v174, v88, v89
	v_mfma_f32_32x32x16_bf16 v[64:79], v[192:195], v[98:101], v[64:79]
	v_max3_f32 v174, v174, v90, v91
	v_max3_f32 v174, v174, v92, v93
	v_max3_f32 v174, v174, v94, v95
	s_nop 8
	v_max3_f32 v174, v174, v64, v65
	v_max3_f32 v174, v174, v66, v67
	v_max3_f32 v174, v174, v68, v69
	v_max3_f32 v174, v174, v70, v71
	v_max3_f32 v174, v174, v72, v73
	v_max3_f32 v174, v174, v74, v75
	v_max3_f32 v174, v174, v76, v77
	v_max3_f32 v174, v174, v78, v79
	v_mov_b32_e32 v180, v174
	s_nop 1
	v_permlane32_swap_b32_e32 v174, v180
	v_max_f32_e32 v180, v180, v180
	v_max_f32_e32 v174, v174, v174
	v_max_f32_e32 v174, v174, v180
	v_sub_f32_e32 v180, v174, v173
	v_max_f32_e32 v174, v181, v174
	v_sub_f32_e32 v181, v173, v174
	v_mul_f32_e32 v181, 0x3dd53b94, v181
	v_exp_f32_e32 v181, v181
	v_cmp_ge_f32_e32 vcc, s33, v180
	s_cmp_eq_u64 vcc, exec
	s_cselect_b64 s[38:39], -1, 0
	v_cndmask_b32_e64 v180, v181, 1.0, s[38:39]
	s_cbranch_scc1 .LBB0_1005
	s_and_saveexec_b64 s[0:1], s[36:37]
	ds_write_b32 v171, v180 offset:51328
	s_or_b64 exec, exec, s[0:1]
	s_waitcnt lgkmcnt(0)
	v_add_u32_e32 v181, v159, v96
	ds_read_b128 v[182:185], v181 offset:51424
	ds_read_b128 v[186:189], v181 offset:51392
	ds_read_b128 v[190:193], v181 offset:51360
	ds_read_b128 v[194:197], v181 offset:51328
	s_waitcnt lgkmcnt(3)
	v_pk_mul_f32 v[12:13], v[12:13], v[182:183]
	s_waitcnt lgkmcnt(2)
	v_pk_mul_f32 v[8:9], v[8:9], v[186:187]
	s_waitcnt lgkmcnt(1)
	v_pk_mul_f32 v[4:5], v[4:5], v[190:191]
	v_pk_mul_f32 v[14:15], v[14:15], v[184:185]
	v_pk_mul_f32 v[10:11], v[10:11], v[188:189]
	v_pk_mul_f32 v[6:7], v[6:7], v[192:193]
	s_waitcnt lgkmcnt(0)
	v_pk_mul_f32 v[2:3], v[2:3], v[196:197]
	v_pk_mul_f32 v[0:1], v[0:1], v[194:195]
	v_pk_mul_f32 v[60:61], v[60:61], v[182:183]
	v_pk_mul_f32 v[56:57], v[56:57], v[186:187]
	v_pk_mul_f32 v[52:53], v[52:53], v[190:191]
	v_pk_mul_f32 v[62:63], v[62:63], v[184:185]
	v_pk_mul_f32 v[58:59], v[58:59], v[188:189]
	v_pk_mul_f32 v[54:55], v[54:55], v[192:193]
	v_pk_mul_f32 v[50:51], v[50:51], v[196:197]
	v_pk_mul_f32 v[48:49], v[48:49], v[194:195]
	v_pk_mul_f32 v[44:45], v[44:45], v[182:183]
	v_pk_mul_f32 v[40:41], v[40:41], v[186:187]
	v_pk_mul_f32 v[36:37], v[36:37], v[190:191]
	v_pk_mul_f32 v[46:47], v[46:47], v[184:185]
	v_pk_mul_f32 v[42:43], v[42:43], v[188:189]
	v_pk_mul_f32 v[38:39], v[38:39], v[192:193]
	v_pk_mul_f32 v[34:35], v[34:35], v[196:197]
	v_pk_mul_f32 v[32:33], v[32:33], v[194:195]
	v_pk_mul_f32 v[28:29], v[28:29], v[182:183]
	v_pk_mul_f32 v[24:25], v[24:25], v[186:187]
	v_pk_mul_f32 v[20:21], v[20:21], v[190:191]
	v_pk_mul_f32 v[30:31], v[30:31], v[184:185]
	v_pk_mul_f32 v[26:27], v[26:27], v[188:189]
	v_pk_mul_f32 v[22:23], v[22:23], v[192:193]
	v_pk_mul_f32 v[18:19], v[18:19], v[196:197]
	v_pk_mul_f32 v[16:17], v[16:17], v[194:195]

; template <int OFF> __device__ __forceinline__ bf16x8 k_read(int kb) { bf16x8 r; asm volatile("ds_read_b128 %0, %1 offset:%2" : "=&v"(r) : "v"(kb), "i"(OFF) : "memory"); return r; }
; #define QK_STEP(D, X, Y, NEXT, N) do { K_WAIT(N, X, Y); \
;         p0 = __builtin_amdgcn_mfma_f32_32x32x16_bf16(X, qr[D], p0, 0, 0, 0); p1 = __builtin_amdgcn_mfma_f32_32x32x16_bf16(Y, qr[D], p1, 0, 0, 0); \
;         if constexpr ((NEXT) < 12) { X = k_read<(NEXT) * 32>(kb); Y = k_read<R1 + (NEXT) * 32>(kb); } } while (0)
; __device__ __forceinline__ void partialSM(f32x16& p0, f32x16& p1, float& m_reg, float& mn, float& alpha) {
;     constexpr float C = SCALE * 1.4426950408889634f;
;     float pmax = p0[0];
; #pragma unroll
;     for (int r = 1; r < 16; ++r) pmax = fmaxf(pmax, p0[r]);
; #pragma unroll
;     for (int r = 0; r < 16; ++r) pmax = fmaxf(pmax, p1[r]);
;     { auto rr = __builtin_amdgcn_permlane32_swap(__float_as_uint(pmax), __float_as_uint(pmax), false, false);
;       pmax = fmaxf(__uint_as_float(rr[0]), __uint_as_float(rr[1])); }
;     if (__builtin_expect(__all(pmax - m_reg <= THR / SCALE), 1)) { mn = m_reg; alpha = 1.f; }
;     else { mn = fmaxf(m_reg, pmax); alpha = __builtin_amdgcn_exp2f((m_reg - mn) * C); m_reg = mn; }
; __device__ __forceinline__ void qkt(f32x16& p0, f32x16& p1, const unsigned char* Ks, const bf16x8* qr, int r32, int hi) {
;     const int kb = (int)(uintptr_t)Ks + r32 * KPITCH + hi * 16;
;     constexpr int R1 = 32 * KPITCH;
;     p0 = f32x16{}; p1 = f32x16{};
;     bf16x8 a0 = k_read<0>(kb), a1 = k_read<R1>(kb), a2 = k_read<32>(kb), a3 = k_read<R1 + 32>(kb), a4 = k_read<64>(kb), a5 = k_read<R1 + 64>(kb);
;     ...
;     QK_STEP(0, a0, a1, 3, 4); QK_STEP(1, a2, a3, 4, 4); QK_STEP(2, a4, a5, 5, 4);
;     QK_STEP(3, a0, a1, 6, 4); QK_STEP(4, a2, a3, 7, 4); QK_STEP(5, a4, a5, 8, 4);
;     QK_STEP(6, a0, a1, 9, 4); QK_STEP(7, a2, a3, 10, 4); QK_STEP(8, a4, a5, 11, 4);
;     QK_STEP(9, a0, a1, 12, 4); QK_STEP(10, a2, a3, 12, 2); QK_STEP(11, a4, a5, 12, 0);
.LBB0_1007:
	s_cmp_lg_u32 0, -1
	s_cselect_b32 s0, 0, 0
	s_addk_i32 s0, 0x6400
	s_waitcnt lgkmcnt(0)
	s_barrier
	v_add_u32_e32 v164, s0, v178
	ds_read_b128 v[64:67], v164 offset:0
	ds_read_b128 v[68:71], v164 offset:0x3200
	s_waitcnt vmcnt(2)
	ds_read_b128 v[146:149], v164 offset:32
	s_waitcnt vmcnt(1)
	ds_read_b128 v[150:153], v164 offset:0x3220
	s_waitcnt vmcnt(0)
	ds_read_b128 v[154:157], v164 offset:64
	ds_read_b128 v[160:163], v164 offset:0x3240
	s_waitcnt lgkmcnt(4)
	s_nop 0
	v_mfma_f32_32x32x16_bf16 v[80:95], v[64:67], v[142:145], 0
	v_mfma_f32_32x32x16_bf16 v[64:79], v[68:71], v[142:145], 0
	ds_read_b128 v[142:145], v164 offset:0x60
	ds_read_b128 v[176:179], v164 offset:0x3260
	s_waitcnt lgkmcnt(4)
	s_nop 0
	v_mfma_f32_32x32x16_bf16 v[80:95], v[146:149], v[138:141], v[80:95]
	v_mfma_f32_32x32x16_bf16 v[64:79], v[150:153], v[138:141], v[64:79]
	ds_read_b128 v[138:141], v164 offset:0x80
	ds_read_b128 v[146:149], v164 offset:0x3280
	s_waitcnt lgkmcnt(4)
	s_nop 0
	v_mfma_f32_32x32x16_bf16 v[80:95], v[154:157], v[134:137], v[80:95]
	v_mfma_f32_32x32x16_bf16 v[64:79], v[160:163], v[134:137], v[64:79]
	ds_read_b128 v[134:137], v164 offset:0xa0
	ds_read_b128 v[150:153], v164 offset:0x32a0
	s_waitcnt lgkmcnt(4)
	s_nop 0
	v_mfma_f32_32x32x16_bf16 v[80:95], v[142:145], v[130:133], v[80:95]
	v_mfma_f32_32x32x16_bf16 v[64:79], v[176:179], v[130:133], v[64:79]
	ds_read_b128 v[130:133], v164 offset:0xc0
	ds_read_b128 v[142:145], v164 offset:0x32c0
	s_waitcnt lgkmcnt(4)
	s_nop 0
	v_mfma_f32_32x32x16_bf16 v[80:95], v[138:141], v[126:129], v[80:95]
	v_mfma_f32_32x32x16_bf16 v[64:79], v[146:149], v[126:129], v[64:79]
	ds_read_b128 v[126:129], v164 offset:0xe0
	ds_read_b128 v[138:141], v164 offset:0x32e0
	s_waitcnt lgkmcnt(4)
	s_nop 0
	v_mfma_f32_32x32x16_bf16 v[80:95], v[134:137], v[122:125], v[80:95]
	v_mfma_f32_32x32x16_bf16 v[64:79], v[150:153], v[122:125], v[64:79]
	ds_read_b128 v[122:125], v164 offset:0x100
	ds_read_b128 v[134:137], v164 offset:0x3300
	s_waitcnt lgkmcnt(4)
	s_nop 0
	v_mfma_f32_32x32x16_bf16 v[80:95], v[130:133], v[118:121], v[80:95]
	v_mfma_f32_32x32x16_bf16 v[64:79], v[142:145], v[118:121], v[64:79]
	ds_read_b128 v[118:121], v164 offset:0x120
	ds_read_b128 v[130:133], v164 offset:0x3320
	s_waitcnt lgkmcnt(4)
	s_nop 0
	v_mfma_f32_32x32x16_bf16 v[80:95], v[126:129], v[114:117], v[80:95]
	v_mfma_f32_32x32x16_bf16 v[64:79], v[138:141], v[114:117], v[64:79]
	ds_read_b128 v[114:117], v164 offset:0x140
	ds_read_b128 v[126:129], v164 offset:0x3340
	s_waitcnt lgkmcnt(4)
	s_nop 0
	v_mfma_f32_32x32x16_bf16 v[80:95], v[122:125], v[110:113], v[80:95]
	v_mfma_f32_32x32x16_bf16 v[64:79], v[134:137], v[110:113], v[64:79]
	ds_read_b128 v[110:113], v164 offset:0x160
	ds_read_b128 v[122:125], v164 offset:0x3360
	s_waitcnt lgkmcnt(4)
	s_waitcnt lgkmcnt(2)
	s_nop 0
	s_waitcnt lgkmcnt(0)
	v_mfma_f32_32x32x16_bf16 v[80:95], v[118:121], v[106:109], v[80:95]
	v_mfma_f32_32x32x16_bf16 v[80:95], v[114:117], v[102:105], v[80:95]
	v_mfma_f32_32x32x16_bf16 v[64:79], v[130:133], v[106:109], v[64:79]
	v_mfma_f32_32x32x16_bf16 v[80:95], v[110:113], v[98:101], v[80:95]
	v_mfma_f32_32x32x16_bf16 v[64:79], v[126:129], v[102:105], v[64:79]
	s_nop 10
	v_max_f32_e32 v106, v81, v81
	v_max_f32_e32 v107, v80, v80
	v_max_f32_e32 v106, v107, v106
	v_max3_f32 v102, v106, v82, v83
	v_max3_f32 v102, v102, v84, v85
	v_max3_f32 v102, v102, v86, v87
	v_max3_f32 v102, v102, v88, v89
	v_mfma_f32_32x32x16_bf16 v[64:79], v[122:125], v[98:101], v[64:79]
	v_max3_f32 v102, v102, v90, v91
	v_max3_f32 v102, v102, v92, v93
	v_max3_f32 v102, v102, v94, v95
	s_nop 8
	v_max3_f32 v98, v102, v64, v65
	v_max3_f32 v98, v98, v66, v67
	v_max3_f32 v98, v98, v68, v69
	v_max3_f32 v98, v98, v70, v71
	v_max3_f32 v98, v98, v72, v73
	v_max3_f32 v98, v98, v74, v75
	v_max3_f32 v98, v98, v76, v77
	v_max3_f32 v98, v98, v78, v79
	v_mov_b32_e32 v99, v98
	s_nop 1
	v_permlane32_swap_b32_e32 v98, v99
	v_max_f32_e32 v99, v99, v99
	v_max_f32_e32 v98, v98, v98
	v_max_f32_e32 v98, v98, v99
	v_max_f32_e32 v99, v173, v173
	v_max_f32_e32 v99, v99, v98
	v_sub_f32_e32 v100, v98, v173
	v_sub_f32_e32 v98, v173, v99
	v_mul_f32_e32 v98, 0x3dd53b94, v98
	v_exp_f32_e32 v98, v98
	v_cmp_ge_f32_e32 vcc, s33, v100
	s_cmp_eq_u64 vcc, exec
	s_cselect_b64 s[38:39], -1, 0
	v_cndmask_b32_e64 v98, v98, 1.0, s[38:39]
	s_cbranch_scc1 .LBB0_1011
	s_and_saveexec_b64 s[0:1], s[36:37]
	ds_write_b32 v171, v98 offset:51328
	s_or_b64 exec, exec, s[0:1]
	s_waitcnt lgkmcnt(0)
	v_add_u32_e32 v112, v159, v96
	ds_read_b128 v[100:103], v112 offset:51424
	ds_read_b128 v[104:107], v112 offset:51392
	ds_read_b128 v[108:111], v112 offset:51360
	ds_read_b128 v[112:115], v112 offset:51328
	s_waitcnt lgkmcnt(3)
	v_pk_mul_f32 v[12:13], v[12:13], v[100:101]
	s_waitcnt lgkmcnt(2)
	v_pk_mul_f32 v[8:9], v[8:9], v[104:105]
	s_waitcnt lgkmcnt(1)
	v_pk_mul_f32 v[4:5], v[4:5], v[108:109]
	v_pk_mul_f32 v[14:15], v[14:15], v[102:103]
	v_pk_mul_f32 v[10:11], v[10:11], v[106:107]
	v_pk_mul_f32 v[6:7], v[6:7], v[110:111]
	s_waitcnt lgkmcnt(0)
	v_pk_mul_f32 v[2:3], v[2:3], v[114:115]
	v_pk_mul_f32 v[0:1], v[0:1], v[112:113]
	v_pk_mul_f32 v[60:61], v[60:61], v[100:101]
	v_pk_mul_f32 v[56:57], v[56:57], v[104:105]
	v_pk_mul_f32 v[52:53], v[52:53], v[108:109]
	v_pk_mul_f32 v[62:63], v[62:63], v[102:103]
	v_pk_mul_f32 v[58:59], v[58:59], v[106:107]
	v_pk_mul_f32 v[54:55], v[54:55], v[110:111]
	v_pk_mul_f32 v[50:51], v[50:51], v[114:115]
	v_pk_mul_f32 v[48:49], v[48:49], v[112:113]
	v_pk_mul_f32 v[44:45], v[44:45], v[100:101]
	v_pk_mul_f32 v[40:41], v[40:41], v[104:105]
	v_pk_mul_f32 v[36:37], v[36:37], v[108:109]
	v_pk_mul_f32 v[46:47], v[46:47], v[102:103]
	v_pk_mul_f32 v[42:43], v[42:43], v[106:107]
	v_pk_mul_f32 v[38:39], v[38:39], v[110:111]
	v_pk_mul_f32 v[34:35], v[34:35], v[114:115]
	v_pk_mul_f32 v[32:33], v[32:33], v[112:113]
	v_pk_mul_f32 v[28:29], v[28:29], v[100:101]
	v_pk_mul_f32 v[24:25], v[24:25], v[104:105]
	v_pk_mul_f32 v[20:21], v[20:21], v[108:109]
	v_pk_mul_f32 v[30:31], v[30:31], v[102:103]
	v_pk_mul_f32 v[26:27], v[26:27], v[106:107]
	v_pk_mul_f32 v[22:23], v[22:23], v[110:111]
	v_pk_mul_f32 v[18:19], v[18:19], v[114:115]
	v_pk_mul_f32 v[16:17], v[16:17], v[112:113]
